# baseline (speedup 1.0000x reference)
.Lgru_loop_a:
	v_mad_u32_u24 v227, v177, s17, v226
	s_nop 0
	s_waitcnt vmcnt(4)
	v_mfma_f32_16x16x32_f16 v[92:95], v[112:115], v[206:209], v[92:95]
	v_exp_f32_e32 v228, v144
	v_exp_f32_e32 v229, v145
	v_exp_f32_e32 v230, v146
	v_exp_f32_e32 v231, v147
	v_exp_f32_e32 v232, v148
	v_exp_f32_e32 v233, v149
	v_exp_f32_e32 v234, v150
	v_exp_f32_e32 v235, v151
	v_mfma_f32_16x16x32_f16 v[92:95], v[108:111], v[210:213], v[92:95]
	v_add_f32_e32 v228, 1.0, v228
	v_add_f32_e32 v229, 1.0, v229
	v_add_f32_e32 v230, 1.0, v230
	v_add_f32_e32 v231, 1.0, v231
	v_add_f32_e32 v232, 1.0, v232
	v_add_f32_e32 v233, 1.0, v233
	v_add_f32_e32 v234, 1.0, v234
	v_add_f32_e32 v235, 1.0, v235
	v_rcp_f32_e32 v228, v228
	v_rcp_f32_e32 v229, v229
	v_rcp_f32_e32 v230, v230
	v_rcp_f32_e32 v231, v231
	v_mfma_f32_16x16x32_f16 v[92:95], v[104:107], v[214:217], v[92:95]
	v_fma_f32 v236, v228, v152, v182
	v_fma_f32 v237, v229, v153, v183
	v_fma_f32 v238, v230, v154, v184
	v_fma_f32 v239, v231, v155, v185
	ds_read_b128 v[222:225], v227 offset:24848
	ds_read_b128 v[186:189], v227 offset:24864
	ds_read_b128 v[182:185], v227 offset:24880
	ds_read_u16 v177, v176 offset:4162
	v_exp_f32_e32 v236, v236
	v_exp_f32_e32 v237, v237
	v_exp_f32_e32 v238, v238
	v_exp_f32_e32 v239, v239
	v_rcp_f32_e32 v232, v232
	v_rcp_f32_e32 v233, v233
	v_mfma_f32_16x16x32_f16 v[92:95], v[100:103], v[218:221], v[92:95]
	global_load_dwordx4 v[112:115], v[166:167], off offset:-2048
	global_load_dwordx4 v[108:111], v[166:167], off offset:-1024
	global_load_dwordx4 v[104:107], v[166:167], off
	global_load_dwordx4 v[100:103], v[166:167], off offset:1024
	v_rcp_f32_e32 v234, v234
	v_rcp_f32_e32 v235, v235
	v_pk_add_f32 v[236:237], v[236:237], 1.0 op_sel_hi:[1,0]
	v_pk_add_f32 v[238:239], v[238:239], 1.0 op_sel_hi:[1,0]
	v_rcp_f32_e32 v236, v236
	v_rcp_f32_e32 v237, v237
	v_rcp_f32_e32 v238, v238
	v_rcp_f32_e32 v239, v239
	v_pk_fma_f32 v[236:237], v[236:237], -2.0, 1.0 op_sel_hi:[1,0,0]
	v_pk_fma_f32 v[238:239], v[238:239], -2.0, 1.0 op_sel_hi:[1,0,0]
	v_pk_add_f32 v[240:241], v[168:169], v[236:237] neg_lo:[0,1] neg_hi:[0,1]
	v_pk_add_f32 v[242:243], v[170:171], v[238:239] neg_lo:[0,1] neg_hi:[0,1]
	v_pk_fma_f32 v[168:169], v[232:233], v[240:241], v[236:237]
	v_pk_fma_f32 v[170:171], v[234:235], v[242:243], v[238:239]
	v_cvt_pk_f16_f32 v244, v168, v169
	v_cvt_pk_f16_f32 v245, v170, v171
	ds_read_b128 v[190:193], v156 offset:0
	ds_read_b128 v[194:197], v156 offset:1024
	ds_read_b128 v[198:201], v156 offset:2048
	ds_read_b128 v[202:205], v156 offset:3072
	ds_write_b64 v163, v[244:245] offset:4096
	s_waitcnt lgkmcnt(4)
	v_mfma_f32_16x16x32_f16 v[124:127], v[12:15], v[190:193], v[116:119]
	v_mfma_f32_16x16x32_f16 v[128:131], v[28:31], v[190:193], v[120:123]
	v_mfma_f32_16x16x32_f16 v[132:135], v[32:35], v[190:193], v[80:83]
	s_waitcnt lgkmcnt(3)
	v_mfma_f32_16x16x32_f16 v[124:127], v[16:19], v[194:197], v[124:127]
	v_mfma_f32_16x16x32_f16 v[128:131], v[48:51], v[194:197], v[128:131]
	v_mfma_f32_16x16x32_f16 v[132:135], v[36:39], v[194:197], v[132:135]
	s_waitcnt lgkmcnt(2)
	v_mfma_f32_16x16x32_f16 v[124:127], v[20:23], v[198:201], v[124:127]
	v_mfma_f32_16x16x32_f16 v[128:131], v[52:55], v[198:201], v[128:131]
	v_mfma_f32_16x16x32_f16 v[132:135], v[40:43], v[198:201], v[132:135]
	s_waitcnt lgkmcnt(1)
	v_mfma_f32_16x16x32_f16 v[124:127], v[24:27], v[202:205], v[124:127]
	v_mfma_f32_16x16x32_f16 v[128:131], v[56:59], v[202:205], v[128:131]
	v_mfma_f32_16x16x32_f16 v[132:135], v[44:47], v[202:205], v[132:135]
	s_waitcnt lgkmcnt(0)
	s_barrier
	v_mad_u32_u24 v227, v178, s17, v226
	s_nop 0
	s_waitcnt vmcnt(4)
	v_mfma_f32_16x16x32_f16 v[96:99], v[72:75], v[190:193], v[96:99]
	v_exp_f32_e32 v228, v124
	v_exp_f32_e32 v229, v125
	v_exp_f32_e32 v230, v126
	v_exp_f32_e32 v231, v127
	v_exp_f32_e32 v232, v128
	v_exp_f32_e32 v233, v129
	v_exp_f32_e32 v234, v130
	v_exp_f32_e32 v235, v131
	v_mfma_f32_16x16x32_f16 v[96:99], v[8:11], v[194:197], v[96:99]
	v_add_f32_e32 v228, 1.0, v228
	v_add_f32_e32 v229, 1.0, v229
	v_add_f32_e32 v230, 1.0, v230
	v_add_f32_e32 v231, 1.0, v231
	v_add_f32_e32 v232, 1.0, v232
	v_add_f32_e32 v233, 1.0, v233
	v_add_f32_e32 v234, 1.0, v234
	v_add_f32_e32 v235, 1.0, v235
	v_rcp_f32_e32 v228, v228
	v_rcp_f32_e32 v229, v229
	v_rcp_f32_e32 v230, v230
	v_rcp_f32_e32 v231, v231
	v_mfma_f32_16x16x32_f16 v[96:99], v[4:7], v[198:201], v[96:99]
	v_fma_f32 v236, v228, v132, v138
	v_fma_f32 v237, v229, v133, v139
	v_fma_f32 v238, v230, v134, v140
	v_fma_f32 v239, v231, v135, v141
	ds_read_b128 v[116:119], v227 offset:24848
	ds_read_b128 v[120:123], v227 offset:24864
	ds_read_b128 v[138:141], v227 offset:24880
	ds_read_u16 v178, v176 offset:4
	v_exp_f32_e32 v236, v236
	v_exp_f32_e32 v237, v237
	v_exp_f32_e32 v238, v238
	v_exp_f32_e32 v239, v239
	v_rcp_f32_e32 v232, v232
	v_rcp_f32_e32 v233, v233
	v_mfma_f32_16x16x32_f16 v[96:99], v[0:3], v[202:205], v[96:99]
	v_rcp_f32_e32 v234, v234
	v_rcp_f32_e32 v235, v235
	v_pk_add_f32 v[236:237], v[236:237], 1.0 op_sel_hi:[1,0]
	v_pk_add_f32 v[238:239], v[238:239], 1.0 op_sel_hi:[1,0]
	v_rcp_f32_e32 v236, v236
	v_rcp_f32_e32 v237, v237
	v_rcp_f32_e32 v238, v238
	v_rcp_f32_e32 v239, v239
	v_pk_fma_f32 v[236:237], v[236:237], -2.0, 1.0 op_sel_hi:[1,0,0]
	v_pk_fma_f32 v[238:239], v[238:239], -2.0, 1.0 op_sel_hi:[1,0,0]
	v_pk_add_f32 v[240:241], v[172:173], v[236:237] neg_lo:[0,1] neg_hi:[0,1]
	v_pk_add_f32 v[242:243], v[174:175], v[238:239] neg_lo:[0,1] neg_hi:[0,1]
	v_pk_fma_f32 v[172:173], v[232:233], v[240:241], v[236:237]
	v_pk_fma_f32 v[174:175], v[234:235], v[242:243], v[238:239]
	v_cvt_pk_f16_f32 v244, v172, v173
	v_cvt_pk_f16_f32 v245, v174, v175
	ds_read_b128 v[206:209], v156 offset:4096
	ds_read_b128 v[210:213], v156 offset:5120
	ds_read_b128 v[214:217], v156 offset:6144
	ds_read_b128 v[218:221], v156 offset:7168
	ds_write_b64 v163, v[244:245]
	s_waitcnt lgkmcnt(4)
	v_mfma_f32_16x16x32_f16 v[144:147], v[12:15], v[206:209], v[222:225]
	v_mfma_f32_16x16x32_f16 v[148:151], v[28:31], v[206:209], v[186:189]
	v_mfma_f32_16x16x32_f16 v[152:155], v[32:35], v[206:209], v[80:83]
	s_waitcnt lgkmcnt(3)
	v_mfma_f32_16x16x32_f16 v[144:147], v[16:19], v[210:213], v[144:147]
	v_mfma_f32_16x16x32_f16 v[148:151], v[48:51], v[210:213], v[148:151]
	v_mfma_f32_16x16x32_f16 v[152:155], v[36:39], v[210:213], v[152:155]
	s_waitcnt lgkmcnt(2)
	v_mfma_f32_16x16x32_f16 v[144:147], v[20:23], v[214:217], v[144:147]
	v_mfma_f32_16x16x32_f16 v[148:151], v[52:55], v[214:217], v[148:151]
	v_mfma_f32_16x16x32_f16 v[152:155], v[40:43], v[214:217], v[152:155]
	s_waitcnt lgkmcnt(1)
	v_mfma_f32_16x16x32_f16 v[144:147], v[24:27], v[218:221], v[144:147]
	v_mfma_f32_16x16x32_f16 v[148:151], v[56:59], v[218:221], v[148:151]
	v_mfma_f32_16x16x32_f16 v[152:155], v[44:47], v[218:221], v[152:155]
	s_waitcnt lgkmcnt(0)
	s_barrier
	v_mad_u32_u24 v227, v177, s17, v226
	s_nop 0
	s_waitcnt vmcnt(4)
	v_mfma_f32_16x16x32_f16 v[92:95], v[72:75], v[206:209], v[92:95]
	v_exp_f32_e32 v228, v144
	v_exp_f32_e32 v229, v145
	v_exp_f32_e32 v230, v146
	v_exp_f32_e32 v231, v147
	v_exp_f32_e32 v232, v148
	v_exp_f32_e32 v233, v149
	v_exp_f32_e32 v234, v150
	v_exp_f32_e32 v235, v151
	v_mfma_f32_16x16x32_f16 v[92:95], v[8:11], v[210:213], v[92:95]
	v_add_f32_e32 v228, 1.0, v228
	v_add_f32_e32 v229, 1.0, v229
	v_add_f32_e32 v230, 1.0, v230
	v_add_f32_e32 v231, 1.0, v231
	v_add_f32_e32 v232, 1.0, v232
	v_add_f32_e32 v233, 1.0, v233
	v_add_f32_e32 v234, 1.0, v234
	v_add_f32_e32 v235, 1.0, v235
	v_rcp_f32_e32 v228, v228
	v_rcp_f32_e32 v229, v229
	v_rcp_f32_e32 v230, v230
	v_rcp_f32_e32 v231, v231
	v_mfma_f32_16x16x32_f16 v[92:95], v[4:7], v[214:217], v[92:95]
	v_fma_f32 v236, v228, v152, v182
	v_fma_f32 v237, v229, v153, v183
	v_fma_f32 v238, v230, v154, v184
	v_fma_f32 v239, v231, v155, v185
	ds_read_b128 v[222:225], v227 offset:24848
	ds_read_b128 v[186:189], v227 offset:24864
	ds_read_b128 v[182:185], v227 offset:24880
	ds_read_u16 v177, v176 offset:4164
	v_exp_f32_e32 v236, v236
	v_exp_f32_e32 v237, v237
	v_exp_f32_e32 v238, v238
	v_exp_f32_e32 v239, v239
	v_rcp_f32_e32 v232, v232
	v_rcp_f32_e32 v233, v233
	v_mfma_f32_16x16x32_f16 v[92:95], v[0:3], v[218:221], v[92:95]
	s_ashr_i32 s9, s8, 31
	s_lshl_b64 s[12:13], s[8:9], 15
	v_lshl_add_u64 v[246:247], v[158:159], 0, s[12:13]
	global_load_dwordx4 v[72:75], v[246:247], off
	global_load_dwordx4 v[8:11], v[246:247], off offset:1024
	global_load_dwordx4 v[4:7], v[246:247], off offset:2048
	global_load_dwordx4 v[0:3], v[246:247], off offset:3072
	v_rcp_f32_e32 v234, v234
	v_rcp_f32_e32 v235, v235
	v_pk_add_f32 v[236:237], v[236:237], 1.0 op_sel_hi:[1,0]
	v_pk_add_f32 v[238:239], v[238:239], 1.0 op_sel_hi:[1,0]
	v_rcp_f32_e32 v236, v236
	v_rcp_f32_e32 v237, v237
	v_rcp_f32_e32 v238, v238
	v_rcp_f32_e32 v239, v239
	v_pk_fma_f32 v[236:237], v[236:237], -2.0, 1.0 op_sel_hi:[1,0,0]
	v_pk_fma_f32 v[238:239], v[238:239], -2.0, 1.0 op_sel_hi:[1,0,0]
	v_pk_add_f32 v[240:241], v[168:169], v[236:237] neg_lo:[0,1] neg_hi:[0,1]
	v_pk_add_f32 v[242:243], v[170:171], v[238:239] neg_lo:[0,1] neg_hi:[0,1]
	v_pk_fma_f32 v[168:169], v[232:233], v[240:241], v[236:237]
	v_pk_fma_f32 v[170:171], v[234:235], v[242:243], v[238:239]
	v_cvt_pk_f16_f32 v244, v168, v169
	v_cvt_pk_f16_f32 v245, v170, v171
	ds_read_b128 v[190:193], v156 offset:0
	ds_read_b128 v[194:197], v156 offset:1024
	ds_read_b128 v[198:201], v156 offset:2048
	ds_read_b128 v[202:205], v156 offset:3072
	ds_write_b64 v163, v[244:245] offset:4096
	s_waitcnt lgkmcnt(4)
	v_mfma_f32_16x16x32_f16 v[124:127], v[12:15], v[190:193], v[116:119]
	v_mfma_f32_16x16x32_f16 v[128:131], v[28:31], v[190:193], v[120:123]
	v_mfma_f32_16x16x32_f16 v[132:135], v[32:35], v[190:193], v[80:83]
	s_waitcnt lgkmcnt(3)
	v_mfma_f32_16x16x32_f16 v[124:127], v[16:19], v[194:197], v[124:127]
	v_mfma_f32_16x16x32_f16 v[128:131], v[48:51], v[194:197], v[128:131]
	v_mfma_f32_16x16x32_f16 v[132:135], v[36:39], v[194:197], v[132:135]
	s_waitcnt lgkmcnt(2)
	v_mfma_f32_16x16x32_f16 v[124:127], v[20:23], v[198:201], v[124:127]
	v_mfma_f32_16x16x32_f16 v[128:131], v[52:55], v[198:201], v[128:131]
	v_mfma_f32_16x16x32_f16 v[132:135], v[40:43], v[198:201], v[132:135]
	s_waitcnt lgkmcnt(1)
	v_mfma_f32_16x16x32_f16 v[124:127], v[24:27], v[202:205], v[124:127]
	v_mfma_f32_16x16x32_f16 v[128:131], v[56:59], v[202:205], v[128:131]
	v_mfma_f32_16x16x32_f16 v[132:135], v[44:47], v[202:205], v[132:135]
	s_waitcnt lgkmcnt(0)
	s_barrier
	v_mad_u32_u24 v227, v178, s17, v226
	s_nop 0
	s_waitcnt vmcnt(4)
	v_mfma_f32_16x16x32_f16 v[96:99], v[112:115], v[190:193], v[96:99]
	v_exp_f32_e32 v228, v124
	v_exp_f32_e32 v229, v125
	v_exp_f32_e32 v230, v126
	v_exp_f32_e32 v231, v127
	v_exp_f32_e32 v232, v128
	v_exp_f32_e32 v233, v129
	v_exp_f32_e32 v234, v130
	v_exp_f32_e32 v235, v131
	v_mfma_f32_16x16x32_f16 v[96:99], v[108:111], v[194:197], v[96:99]
	v_add_f32_e32 v228, 1.0, v228
	v_add_f32_e32 v229, 1.0, v229
	v_add_f32_e32 v230, 1.0, v230
	v_add_f32_e32 v231, 1.0, v231
	v_add_f32_e32 v232, 1.0, v232
	v_add_f32_e32 v233, 1.0, v233
	v_add_f32_e32 v234, 1.0, v234
	v_add_f32_e32 v235, 1.0, v235
	v_rcp_f32_e32 v228, v228
	v_rcp_f32_e32 v229, v229
	v_rcp_f32_e32 v230, v230
	v_rcp_f32_e32 v231, v231
	v_mfma_f32_16x16x32_f16 v[96:99], v[104:107], v[198:201], v[96:99]
	v_fma_f32 v236, v228, v132, v138
	v_fma_f32 v237, v229, v133, v139
	v_fma_f32 v238, v230, v134, v140
	v_fma_f32 v239, v231, v135, v141
	ds_read_b128 v[116:119], v227 offset:24848
	ds_read_b128 v[120:123], v227 offset:24864
	ds_read_b128 v[138:141], v227 offset:24880
	ds_read_u16 v178, v176 offset:6
	v_exp_f32_e32 v236, v236
	v_exp_f32_e32 v237, v237
	v_exp_f32_e32 v238, v238
	v_exp_f32_e32 v239, v239
	v_rcp_f32_e32 v232, v232
	v_rcp_f32_e32 v233, v233
	v_mfma_f32_16x16x32_f16 v[96:99], v[100:103], v[202:205], v[96:99]
	v_rcp_f32_e32 v234, v234
	v_rcp_f32_e32 v235, v235
	v_pk_add_f32 v[236:237], v[236:237], 1.0 op_sel_hi:[1,0]
	v_pk_add_f32 v[238:239], v[238:239], 1.0 op_sel_hi:[1,0]
	v_rcp_f32_e32 v236, v236
	v_rcp_f32_e32 v237, v237
	v_rcp_f32_e32 v238, v238
	v_rcp_f32_e32 v239, v239
	v_pk_fma_f32 v[236:237], v[236:237], -2.0, 1.0 op_sel_hi:[1,0,0]
	v_pk_fma_f32 v[238:239], v[238:239], -2.0, 1.0 op_sel_hi:[1,0,0]
	v_pk_add_f32 v[240:241], v[172:173], v[236:237] neg_lo:[0,1] neg_hi:[0,1]
	v_pk_add_f32 v[242:243], v[174:175], v[238:239] neg_lo:[0,1] neg_hi:[0,1]
	v_pk_fma_f32 v[172:173], v[232:233], v[240:241], v[236:237]
	v_pk_fma_f32 v[174:175], v[234:235], v[242:243], v[238:239]
	v_cvt_pk_f16_f32 v244, v172, v173
	v_cvt_pk_f16_f32 v245, v174, v175
	ds_read_b128 v[206:209], v156 offset:4096
	ds_read_b128 v[210:213], v156 offset:5120
	ds_read_b128 v[214:217], v156 offset:6144
	ds_read_b128 v[218:221], v156 offset:7168
	ds_write_b64 v163, v[244:245]
	s_waitcnt lgkmcnt(4)
	v_mfma_f32_16x16x32_f16 v[144:147], v[12:15], v[206:209], v[222:225]
	v_mfma_f32_16x16x32_f16 v[148:151], v[28:31], v[206:209], v[186:189]
	v_mfma_f32_16x16x32_f16 v[152:155], v[32:35], v[206:209], v[80:83]
	s_waitcnt lgkmcnt(3)
	v_mfma_f32_16x16x32_f16 v[144:147], v[16:19], v[210:213], v[144:147]
	v_mfma_f32_16x16x32_f16 v[148:151], v[48:51], v[210:213], v[148:151]
	v_mfma_f32_16x16x32_f16 v[152:155], v[36:39], v[210:213], v[152:155]
	s_waitcnt lgkmcnt(2)
	v_mfma_f32_16x16x32_f16 v[144:147], v[20:23], v[214:217], v[144:147]
	v_mfma_f32_16x16x32_f16 v[148:151], v[52:55], v[214:217], v[148:151]
	v_mfma_f32_16x16x32_f16 v[152:155], v[40:43], v[214:217], v[152:155]
	s_waitcnt lgkmcnt(1)
	v_mfma_f32_16x16x32_f16 v[144:147], v[24:27], v[218:221], v[144:147]
	v_mfma_f32_16x16x32_f16 v[148:151], v[56:59], v[218:221], v[148:151]
	v_mfma_f32_16x16x32_f16 v[152:155], v[44:47], v[218:221], v[152:155]
	s_add_i32 s5, s5, 2
	s_add_i32 s8, s8, s4
	v_add_u32_e32 v176, 4, v176
	v_lshl_add_u64 v[166:167], v[166:167], 0, s[6:7]
	s_cmpk_gt_u32 s5, 0x7d
	s_waitcnt lgkmcnt(0)
	s_barrier
	s_cbranch_scc0 .Lgru_loop_a
	s_branch .Lgru_tail
.Lgru_loop_b:
.Lgru_loop_b2:
	ds_read_b128 v[190:193], v156 offset:0
	ds_read_b128 v[194:197], v156 offset:1024
	ds_read_b128 v[198:201], v156 offset:2048
	ds_read_b128 v[202:205], v156 offset:3072
	global_load_dwordx4 v[112:115], v[166:167], off offset:-2048
	global_load_dwordx4 v[108:111], v[166:167], off offset:-1024
	global_load_dwordx4 v[104:107], v[166:167], off
	global_load_dwordx4 v[100:103], v[166:167], off offset:1024
	s_waitcnt lgkmcnt(3)
	v_mfma_f32_16x16x32_f16 v[124:127], v[12:15], v[190:193], v[116:119]
	v_mfma_f32_16x16x32_f16 v[128:131], v[28:31], v[190:193], v[120:123]
	v_mfma_f32_16x16x32_f16 v[132:135], v[32:35], v[190:193], v[80:83]
	s_waitcnt lgkmcnt(2)
	v_mfma_f32_16x16x32_f16 v[124:127], v[16:19], v[194:197], v[124:127]
	v_mfma_f32_16x16x32_f16 v[128:131], v[48:51], v[194:197], v[128:131]
	v_mfma_f32_16x16x32_f16 v[132:135], v[36:39], v[194:197], v[132:135]
	s_waitcnt lgkmcnt(1)
	v_mfma_f32_16x16x32_f16 v[124:127], v[20:23], v[198:201], v[124:127]
	v_mfma_f32_16x16x32_f16 v[128:131], v[52:55], v[198:201], v[128:131]
	v_mfma_f32_16x16x32_f16 v[132:135], v[40:43], v[198:201], v[132:135]
	s_waitcnt lgkmcnt(0)
	v_mfma_f32_16x16x32_f16 v[124:127], v[24:27], v[202:205], v[124:127]
	v_mfma_f32_16x16x32_f16 v[128:131], v[56:59], v[202:205], v[128:131]
	v_mfma_f32_16x16x32_f16 v[132:135], v[44:47], v[202:205], v[132:135]
	v_exp_f32_e32 v228, v144
	v_exp_f32_e32 v229, v145
	v_exp_f32_e32 v230, v146
	v_exp_f32_e32 v231, v147
	v_exp_f32_e32 v232, v148
	v_exp_f32_e32 v233, v149
	v_exp_f32_e32 v234, v150
	v_exp_f32_e32 v235, v151
	v_add_f32_e32 v228, 1.0, v228
	v_add_f32_e32 v229, 1.0, v229
	v_add_f32_e32 v230, 1.0, v230
	v_add_f32_e32 v231, 1.0, v231
	v_add_f32_e32 v232, 1.0, v232
	v_add_f32_e32 v233, 1.0, v233
	v_add_f32_e32 v234, 1.0, v234
	v_add_f32_e32 v235, 1.0, v235
	v_rcp_f32_e32 v228, v228
	v_rcp_f32_e32 v229, v229
	v_rcp_f32_e32 v230, v230
	v_rcp_f32_e32 v231, v231
	v_fma_f32 v236, v228, v152, v182
	v_fma_f32 v237, v229, v153, v183
	v_fma_f32 v238, v230, v154, v184
	v_fma_f32 v239, v231, v155, v185
	v_mad_u32_u24 v227, v177, s17, v226
	ds_read_b128 v[222:225], v227 offset:24848
	ds_read_b128 v[186:189], v227 offset:24864
	ds_read_b128 v[182:185], v227 offset:24880
	ds_read_u16 v177, v176 offset:4162
	v_exp_f32_e32 v236, v236
	v_exp_f32_e32 v237, v237
	v_exp_f32_e32 v238, v238
	v_exp_f32_e32 v239, v239
	v_rcp_f32_e32 v232, v232
	v_rcp_f32_e32 v233, v233
	v_rcp_f32_e32 v234, v234
	v_rcp_f32_e32 v235, v235
	v_pk_add_f32 v[236:237], v[236:237], 1.0 op_sel_hi:[1,0]
	v_pk_add_f32 v[238:239], v[238:239], 1.0 op_sel_hi:[1,0]
	v_rcp_f32_e32 v236, v236
	v_rcp_f32_e32 v237, v237
	v_rcp_f32_e32 v238, v238
	v_rcp_f32_e32 v239, v239
	v_pk_fma_f32 v[236:237], v[236:237], -2.0, 1.0 op_sel_hi:[1,0,0]
	v_pk_fma_f32 v[238:239], v[238:239], -2.0, 1.0 op_sel_hi:[1,0,0]
	v_pk_add_f32 v[240:241], v[168:169], v[236:237] neg_lo:[0,1] neg_hi:[0,1]
	v_pk_add_f32 v[242:243], v[170:171], v[238:239] neg_lo:[0,1] neg_hi:[0,1]
	v_pk_fma_f32 v[168:169], v[232:233], v[240:241], v[236:237]
	v_pk_fma_f32 v[170:171], v[234:235], v[242:243], v[238:239]
	v_cvt_pk_f16_f32 v244, v168, v169
	v_cvt_pk_f16_f32 v245, v170, v171
	ds_write_b64 v163, v[244:245] offset:4096
	s_waitcnt vmcnt(4)
	v_mfma_f32_16x16x32_f16 v[96:99], v[72:75], v[190:193], v[96:99]
	v_mfma_f32_16x16x32_f16 v[96:99], v[8:11], v[194:197], v[96:99]
	v_mfma_f32_16x16x32_f16 v[96:99], v[4:7], v[198:201], v[96:99]
	v_mfma_f32_16x16x32_f16 v[96:99], v[0:3], v[202:205], v[96:99]
	s_waitcnt lgkmcnt(0)
	s_barrier
	ds_read_b128 v[206:209], v156 offset:4096
	ds_read_b128 v[210:213], v156 offset:5120
	ds_read_b128 v[214:217], v156 offset:6144
	ds_read_b128 v[218:221], v156 offset:7168
	s_waitcnt lgkmcnt(3)
	v_mfma_f32_16x16x32_f16 v[144:147], v[12:15], v[206:209], v[222:225]
	v_mfma_f32_16x16x32_f16 v[148:151], v[28:31], v[206:209], v[186:189]
	v_mfma_f32_16x16x32_f16 v[152:155], v[32:35], v[206:209], v[80:83]
	s_waitcnt lgkmcnt(2)
	v_mfma_f32_16x16x32_f16 v[144:147], v[16:19], v[210:213], v[144:147]
	v_mfma_f32_16x16x32_f16 v[148:151], v[48:51], v[210:213], v[148:151]
	v_mfma_f32_16x16x32_f16 v[152:155], v[36:39], v[210:213], v[152:155]
	s_waitcnt lgkmcnt(1)
	v_mfma_f32_16x16x32_f16 v[144:147], v[20:23], v[214:217], v[144:147]
	v_mfma_f32_16x16x32_f16 v[148:151], v[52:55], v[214:217], v[148:151]
	v_mfma_f32_16x16x32_f16 v[152:155], v[40:43], v[214:217], v[152:155]
	s_waitcnt lgkmcnt(0)
	v_mfma_f32_16x16x32_f16 v[144:147], v[24:27], v[218:221], v[144:147]
	v_mfma_f32_16x16x32_f16 v[148:151], v[56:59], v[218:221], v[148:151]
	v_mfma_f32_16x16x32_f16 v[152:155], v[44:47], v[218:221], v[152:155]
	v_exp_f32_e32 v228, v124
	v_exp_f32_e32 v229, v125
	v_exp_f32_e32 v230, v126
	v_exp_f32_e32 v231, v127
	v_exp_f32_e32 v232, v128
	v_exp_f32_e32 v233, v129
	v_exp_f32_e32 v234, v130
	v_exp_f32_e32 v235, v131
	v_add_f32_e32 v228, 1.0, v228
	v_add_f32_e32 v229, 1.0, v229
	v_add_f32_e32 v230, 1.0, v230
	v_add_f32_e32 v231, 1.0, v231
	v_add_f32_e32 v232, 1.0, v232
	v_add_f32_e32 v233, 1.0, v233
	v_add_f32_e32 v234, 1.0, v234
	v_add_f32_e32 v235, 1.0, v235
	v_rcp_f32_e32 v228, v228
	v_rcp_f32_e32 v229, v229
	v_rcp_f32_e32 v230, v230
	v_rcp_f32_e32 v231, v231
	v_fma_f32 v236, v228, v132, v138
	v_fma_f32 v237, v229, v133, v139
	v_fma_f32 v238, v230, v134, v140
	v_fma_f32 v239, v231, v135, v141
	v_mad_u32_u24 v227, v178, s17, v226
	ds_read_b128 v[116:119], v227 offset:24848
	ds_read_b128 v[120:123], v227 offset:24864
	ds_read_b128 v[138:141], v227 offset:24880
	ds_read_u16 v178, v176 offset:4
	v_exp_f32_e32 v236, v236
	v_exp_f32_e32 v237, v237
	v_exp_f32_e32 v238, v238
	v_exp_f32_e32 v239, v239
	v_rcp_f32_e32 v232, v232
	v_rcp_f32_e32 v233, v233
	v_rcp_f32_e32 v234, v234
	v_rcp_f32_e32 v235, v235
	v_pk_add_f32 v[236:237], v[236:237], 1.0 op_sel_hi:[1,0]
	v_pk_add_f32 v[238:239], v[238:239], 1.0 op_sel_hi:[1,0]
	v_rcp_f32_e32 v236, v236
	v_rcp_f32_e32 v237, v237
	v_rcp_f32_e32 v238, v238
	v_rcp_f32_e32 v239, v239
	v_pk_fma_f32 v[236:237], v[236:237], -2.0, 1.0 op_sel_hi:[1,0,0]
	v_pk_fma_f32 v[238:239], v[238:239], -2.0, 1.0 op_sel_hi:[1,0,0]
	v_pk_add_f32 v[240:241], v[172:173], v[236:237] neg_lo:[0,1] neg_hi:[0,1]
	v_pk_add_f32 v[242:243], v[174:175], v[238:239] neg_lo:[0,1] neg_hi:[0,1]
	v_pk_fma_f32 v[172:173], v[232:233], v[240:241], v[236:237]
	v_pk_fma_f32 v[174:175], v[234:235], v[242:243], v[238:239]
	v_cvt_pk_f16_f32 v244, v172, v173
	v_cvt_pk_f16_f32 v245, v174, v175
	ds_write_b64 v163, v[244:245]
	s_waitcnt vmcnt(4)
	v_mfma_f32_16x16x32_f16 v[92:95], v[72:75], v[206:209], v[92:95]
	v_mfma_f32_16x16x32_f16 v[92:95], v[8:11], v[210:213], v[92:95]
	v_mfma_f32_16x16x32_f16 v[92:95], v[4:7], v[214:217], v[92:95]
	v_mfma_f32_16x16x32_f16 v[92:95], v[0:3], v[218:221], v[92:95]
	s_waitcnt lgkmcnt(0)
	s_barrier
	ds_read_b128 v[190:193], v156 offset:0
	ds_read_b128 v[194:197], v156 offset:1024
	ds_read_b128 v[198:201], v156 offset:2048
	ds_read_b128 v[202:205], v156 offset:3072
	s_ashr_i32 s9, s8, 31
	s_lshl_b64 s[12:13], s[8:9], 15
	v_lshl_add_u64 v[246:247], v[158:159], 0, s[12:13]
	global_load_dwordx4 v[72:75], v[246:247], off
	global_load_dwordx4 v[8:11], v[246:247], off offset:1024
	global_load_dwordx4 v[4:7], v[246:247], off offset:2048
	global_load_dwordx4 v[0:3], v[246:247], off offset:3072
	s_waitcnt lgkmcnt(3)
	v_mfma_f32_16x16x32_f16 v[124:127], v[12:15], v[190:193], v[116:119]
	v_mfma_f32_16x16x32_f16 v[128:131], v[28:31], v[190:193], v[120:123]
	v_mfma_f32_16x16x32_f16 v[132:135], v[32:35], v[190:193], v[80:83]
	s_waitcnt lgkmcnt(2)
	v_mfma_f32_16x16x32_f16 v[124:127], v[16:19], v[194:197], v[124:127]
	v_mfma_f32_16x16x32_f16 v[128:131], v[48:51], v[194:197], v[128:131]
	v_mfma_f32_16x16x32_f16 v[132:135], v[36:39], v[194:197], v[132:135]
	s_waitcnt lgkmcnt(1)
	v_mfma_f32_16x16x32_f16 v[124:127], v[20:23], v[198:201], v[124:127]
	v_mfma_f32_16x16x32_f16 v[128:131], v[52:55], v[198:201], v[128:131]
	v_mfma_f32_16x16x32_f16 v[132:135], v[40:43], v[198:201], v[132:135]
	s_waitcnt lgkmcnt(0)
	v_mfma_f32_16x16x32_f16 v[124:127], v[24:27], v[202:205], v[124:127]
	v_mfma_f32_16x16x32_f16 v[128:131], v[56:59], v[202:205], v[128:131]
	v_mfma_f32_16x16x32_f16 v[132:135], v[44:47], v[202:205], v[132:135]
	v_exp_f32_e32 v228, v144
	v_exp_f32_e32 v229, v145
	v_exp_f32_e32 v230, v146
	v_exp_f32_e32 v231, v147
	v_exp_f32_e32 v232, v148
	v_exp_f32_e32 v233, v149
	v_exp_f32_e32 v234, v150
	v_exp_f32_e32 v235, v151
	v_add_f32_e32 v228, 1.0, v228
	v_add_f32_e32 v229, 1.0, v229
	v_add_f32_e32 v230, 1.0, v230
	v_add_f32_e32 v231, 1.0, v231
	v_add_f32_e32 v232, 1.0, v232
	v_add_f32_e32 v233, 1.0, v233
	v_add_f32_e32 v234, 1.0, v234
	v_add_f32_e32 v235, 1.0, v235
	v_rcp_f32_e32 v228, v228
	v_rcp_f32_e32 v229, v229
	v_rcp_f32_e32 v230, v230
	v_rcp_f32_e32 v231, v231
	v_fma_f32 v236, v228, v152, v182
	v_fma_f32 v237, v229, v153, v183
	v_fma_f32 v238, v230, v154, v184
	v_fma_f32 v239, v231, v155, v185
	v_mad_u32_u24 v227, v177, s17, v226
	ds_read_b128 v[222:225], v227 offset:24848
	ds_read_b128 v[186:189], v227 offset:24864
	ds_read_b128 v[182:185], v227 offset:24880
	ds_read_u16 v177, v176 offset:4164
	v_exp_f32_e32 v236, v236
	v_exp_f32_e32 v237, v237
	v_exp_f32_e32 v238, v238
	v_exp_f32_e32 v239, v239
	v_rcp_f32_e32 v232, v232
	v_rcp_f32_e32 v233, v233
	v_rcp_f32_e32 v234, v234
	v_rcp_f32_e32 v235, v235
	v_pk_add_f32 v[236:237], v[236:237], 1.0 op_sel_hi:[1,0]
	v_pk_add_f32 v[238:239], v[238:239], 1.0 op_sel_hi:[1,0]
	v_rcp_f32_e32 v236, v236
	v_rcp_f32_e32 v237, v237
	v_rcp_f32_e32 v238, v238
	v_rcp_f32_e32 v239, v239
	v_pk_fma_f32 v[236:237], v[236:237], -2.0, 1.0 op_sel_hi:[1,0,0]
	v_pk_fma_f32 v[238:239], v[238:239], -2.0, 1.0 op_sel_hi:[1,0,0]
	v_pk_add_f32 v[240:241], v[168:169], v[236:237] neg_lo:[0,1] neg_hi:[0,1]
	v_pk_add_f32 v[242:243], v[170:171], v[238:239] neg_lo:[0,1] neg_hi:[0,1]
	v_pk_fma_f32 v[168:169], v[232:233], v[240:241], v[236:237]
	v_pk_fma_f32 v[170:171], v[234:235], v[242:243], v[238:239]
	v_cvt_pk_f16_f32 v244, v168, v169
	v_cvt_pk_f16_f32 v245, v170, v171
	ds_write_b64 v163, v[244:245] offset:4096
	s_waitcnt vmcnt(4)
	v_mfma_f32_16x16x32_f16 v[96:99], v[112:115], v[190:193], v[96:99]
	v_mfma_f32_16x16x32_f16 v[96:99], v[108:111], v[194:197], v[96:99]
	v_mfma_f32_16x16x32_f16 v[96:99], v[104:107], v[198:201], v[96:99]
	v_mfma_f32_16x16x32_f16 v[96:99], v[100:103], v[202:205], v[96:99]
	s_waitcnt lgkmcnt(0)
	s_barrier
	ds_read_b128 v[206:209], v156 offset:4096
	ds_read_b128 v[210:213], v156 offset:5120
	ds_read_b128 v[214:217], v156 offset:6144
	ds_read_b128 v[218:221], v156 offset:7168
	s_waitcnt lgkmcnt(3)
	v_mfma_f32_16x16x32_f16 v[144:147], v[12:15], v[206:209], v[222:225]
	v_mfma_f32_16x16x32_f16 v[148:151], v[28:31], v[206:209], v[186:189]
	v_mfma_f32_16x16x32_f16 v[152:155], v[32:35], v[206:209], v[80:83]
	s_waitcnt lgkmcnt(2)
	v_mfma_f32_16x16x32_f16 v[144:147], v[16:19], v[210:213], v[144:147]
	v_mfma_f32_16x16x32_f16 v[148:151], v[48:51], v[210:213], v[148:151]
	v_mfma_f32_16x16x32_f16 v[152:155], v[36:39], v[210:213], v[152:155]
	s_waitcnt lgkmcnt(1)
	v_mfma_f32_16x16x32_f16 v[144:147], v[20:23], v[214:217], v[144:147]
	v_mfma_f32_16x16x32_f16 v[148:151], v[52:55], v[214:217], v[148:151]
	v_mfma_f32_16x16x32_f16 v[152:155], v[40:43], v[214:217], v[152:155]
	s_waitcnt lgkmcnt(0)
	v_mfma_f32_16x16x32_f16 v[144:147], v[24:27], v[218:221], v[144:147]
	v_mfma_f32_16x16x32_f16 v[148:151], v[56:59], v[218:221], v[148:151]
	v_mfma_f32_16x16x32_f16 v[152:155], v[44:47], v[218:221], v[152:155]
	v_exp_f32_e32 v228, v124
	v_exp_f32_e32 v229, v125
	v_exp_f32_e32 v230, v126
	v_exp_f32_e32 v231, v127
	v_exp_f32_e32 v232, v128
	v_exp_f32_e32 v233, v129
	v_exp_f32_e32 v234, v130
	v_exp_f32_e32 v235, v131
	v_add_f32_e32 v228, 1.0, v228
	v_add_f32_e32 v229, 1.0, v229
	v_add_f32_e32 v230, 1.0, v230
	v_add_f32_e32 v231, 1.0, v231
	v_add_f32_e32 v232, 1.0, v232
	v_add_f32_e32 v233, 1.0, v233
	v_add_f32_e32 v234, 1.0, v234
	v_add_f32_e32 v235, 1.0, v235
	v_rcp_f32_e32 v228, v228
	v_rcp_f32_e32 v229, v229
	v_rcp_f32_e32 v230, v230
	v_rcp_f32_e32 v231, v231
	v_fma_f32 v236, v228, v132, v138
	v_fma_f32 v237, v229, v133, v139
	v_fma_f32 v238, v230, v134, v140
	v_fma_f32 v239, v231, v135, v141
	v_mad_u32_u24 v227, v178, s17, v226
	ds_read_b128 v[116:119], v227 offset:24848
	ds_read_b128 v[120:123], v227 offset:24864
	ds_read_b128 v[138:141], v227 offset:24880
	ds_read_u16 v178, v176 offset:6
	v_exp_f32_e32 v236, v236
	v_exp_f32_e32 v237, v237
	v_exp_f32_e32 v238, v238
	v_exp_f32_e32 v239, v239
	v_rcp_f32_e32 v232, v232
	v_rcp_f32_e32 v233, v233
	v_rcp_f32_e32 v234, v234
	v_rcp_f32_e32 v235, v235
	v_pk_add_f32 v[236:237], v[236:237], 1.0 op_sel_hi:[1,0]
	v_pk_add_f32 v[238:239], v[238:239], 1.0 op_sel_hi:[1,0]
	v_rcp_f32_e32 v236, v236
	v_rcp_f32_e32 v237, v237
	v_rcp_f32_e32 v238, v238
	v_rcp_f32_e32 v239, v239
	v_pk_fma_f32 v[236:237], v[236:237], -2.0, 1.0 op_sel_hi:[1,0,0]
	v_pk_fma_f32 v[238:239], v[238:239], -2.0, 1.0 op_sel_hi:[1,0,0]
	v_pk_add_f32 v[240:241], v[172:173], v[236:237] neg_lo:[0,1] neg_hi:[0,1]
	v_pk_add_f32 v[242:243], v[174:175], v[238:239] neg_lo:[0,1] neg_hi:[0,1]
	v_pk_fma_f32 v[172:173], v[232:233], v[240:241], v[236:237]
	v_pk_fma_f32 v[174:175], v[234:235], v[242:243], v[238:239]
	v_cvt_pk_f16_f32 v244, v172, v173
	v_cvt_pk_f16_f32 v245, v174, v175
	ds_write_b64 v163, v[244:245]
	s_waitcnt vmcnt(4)
	v_mfma_f32_16x16x32_f16 v[92:95], v[112:115], v[206:209], v[92:95]
	v_mfma_f32_16x16x32_f16 v[92:95], v[108:111], v[210:213], v[92:95]
	v_mfma_f32_16x16x32_f16 v[92:95], v[104:107], v[214:217], v[92:95]
	v_mfma_f32_16x16x32_f16 v[92:95], v[100:103], v[218:221], v[92:95]
	s_add_i32 s5, s5, 2
	s_add_i32 s8, s8, s4
	v_add_u32_e32 v176, 4, v176
	v_lshl_add_u64 v[166:167], v[166:167], 0, s[6:7]
	s_cmpk_gt_u32 s5, 0x7d
	s_waitcnt lgkmcnt(0)
	s_barrier
	s_cbranch_scc0 .Lgru_loop_b2
	s_waitcnt vmcnt(0)
	s_branch .Lgru_tail2
